# DSA attention unit set-up de-waterfall (mask rows in two groups of four loads, bucket-id load shares a round trip, deferred pre-claim wait); carry chains padded
# speedup vs baseline: 1.0132x; 1.0132x over previous
.LBB0_1636:
	s_mov_b64 s[36:37], vcc
	s_and_saveexec_b64 s[10:11], vcc
	v_ashrrev_i32_e32 v90, 8, v20
	v_lshlrev_b32_e32 v90, 10, v90
	v_mov_b32_e32 v91, v3
	v_lshl_add_u64 v[90:91], v[4:5], 0, v[90:91]
	v_add_co_u32_e32 v98, vcc, 0x1000, v90
	s_nop 1
	v_addc_co_u32_e32 v99, vcc, 0, v91, vcc
	global_load_dwordx4 v[100:103], v[90:91], off
	global_load_dwordx4 v[104:107], v[90:91], off offset:2048
	global_load_dwordx4 v[108:111], v[98:99], off
	global_load_dwordx4 v[112:115], v[98:99], off offset:2048
	s_mov_b64 exec, s[10:11]
	v_cmp_gt_i32_e32 vcc, 0x84, v233
	s_and_saveexec_b64 s[10:11], vcc
	v_lshlrev_b32_e32 v92, 4, v233
	v_mov_b32_e32 v93, v3
	v_add_u32_e32 v96, s94, v92
	v_lshl_add_u64 v[92:93], s[26:27], 0, v[92:93]
	global_load_dwordx4 v[92:95], v[92:93], off
	s_waitcnt vmcnt(0)
	ds_write_b128 v96, v[92:95]
	s_mov_b64 exec, s[10:11]
	s_and_saveexec_b64 s[10:11], s[36:37]
	v_ashrrev_i32_e32 v7, 6, v20
	v_lshlrev_b32_e32 v12, 4, v7
	s_movk_i32 s13, 0x104
	v_mad_u32_u24 v13, v7, s13, v6
	v_add_co_u32_e32 v90, vcc, 0x2000, v90
	s_nop 1
	v_addc_co_u32_e32 v91, vcc, 0, v91, vcc
	v_add_co_u32_e32 v98, vcc, 0x2000, v98
	s_nop 1
	v_addc_co_u32_e32 v99, vcc, 0, v99, vcc
	s_waitcnt vmcnt(0)
	v_lshrrev_b64 v[8:9], v12, v[100:101]
	v_lshrrev_b64 v[10:11], v12, v[102:103]
	v_and_b32_e32 v8, 0xffff, v8
	v_lshl_or_b32 v100, v10, 16, v8
	ds_write_b32 v13, v100 offset:0
	v_lshrrev_b64 v[8:9], v12, v[104:105]
	v_lshrrev_b64 v[10:11], v12, v[106:107]
	v_and_b32_e32 v8, 0xffff, v8
	v_lshl_or_b32 v104, v10, 16, v8
	ds_write_b32 v13, v104 offset:2080
	v_lshrrev_b64 v[8:9], v12, v[108:109]
	v_lshrrev_b64 v[10:11], v12, v[110:111]
	v_and_b32_e32 v8, 0xffff, v8
	v_lshl_or_b32 v108, v10, 16, v8
	ds_write_b32 v13, v108 offset:4160
	v_lshrrev_b64 v[8:9], v12, v[112:113]
	v_lshrrev_b64 v[10:11], v12, v[114:115]
	v_and_b32_e32 v8, 0xffff, v8
	v_lshl_or_b32 v112, v10, 16, v8
	ds_write_b32 v13, v112 offset:6240
	global_load_dwordx4 v[100:103], v[90:91], off
	global_load_dwordx4 v[104:107], v[90:91], off offset:2048
	global_load_dwordx4 v[108:111], v[98:99], off
	global_load_dwordx4 v[112:115], v[98:99], off offset:2048
	s_waitcnt vmcnt(0)
	v_lshrrev_b64 v[8:9], v12, v[100:101]
	v_lshrrev_b64 v[10:11], v12, v[102:103]
	v_and_b32_e32 v8, 0xffff, v8
	v_lshl_or_b32 v100, v10, 16, v8
	ds_write_b32 v13, v100 offset:8320
	v_lshrrev_b64 v[8:9], v12, v[104:105]
	v_lshrrev_b64 v[10:11], v12, v[106:107]
	v_and_b32_e32 v8, 0xffff, v8
	v_lshl_or_b32 v104, v10, 16, v8
	ds_write_b32 v13, v104 offset:10400
	v_lshrrev_b64 v[8:9], v12, v[108:109]
	v_lshrrev_b64 v[10:11], v12, v[110:111]
	v_and_b32_e32 v8, 0xffff, v8
	v_lshl_or_b32 v108, v10, 16, v8
	ds_write_b32 v13, v108 offset:12480
	v_lshrrev_b64 v[8:9], v12, v[112:113]
	v_lshrrev_b64 v[10:11], v12, v[114:115]
	v_and_b32_e32 v8, 0xffff, v8
	v_lshl_or_b32 v112, v10, 16, v8
	ds_write_b32 v13, v112 offset:14560
	s_mov_b64 exec, s[10:11]
